# branchnorm: second-pass row loads issued during the first pass into spare registers (software prefetch), waits counted (vmcnt 8)
# speedup vs baseline: 1.0071x; 1.0038x over previous
.LBB0_1218:
	s_lshr_b32 s18, s16, 6
	s_lshl_b32 s16, s16, 6
	s_mulk_i32 s18, 0x1100
	s_and_b32 s16, s16, 0xfc0
	s_add_i32 s18, s18, s16
	v_add_u32_e32 v103, s18, v93
	v_add3_u32 v104, s17, v91, v94
	s_mov_b32 s20, 0
	s_mov_b64 s[16:17], -1
	s_mov_b32 s100, 0x2000
	s_mov_b32 s101, 0
	s_branch .LBB0_1220

.LBB0_1222:
	s_or_saveexec_b64 s[18:19], s[18:19]
	v_or_b32_e32 v70, s20, v103
	v_ashrrev_i32_e32 v71, 31, v70
	v_lshlrev_b64 v[34:35], 11, v[70:71]
	v_lshl_add_u64 v[76:77], v[68:69], 0, v[34:35]
	s_xor_b64 exec, exec, s[18:19]
	s_cbranch_execz .LBB0_1224
	s_cmp_lg_u32 s20, 0
	s_cbranch_scc1 .Lbn_mv0
	global_load_dwordx4 v[58:61], v[76:77], off offset:16
	global_load_dwordx4 v[62:65], v[76:77], off
	s_branch .LBB0_1224
.Lbn_mv0:
	s_waitcnt vmcnt(8)
	v_mov_b32_e32 v58, v238
	v_mov_b32_e32 v59, v239
	v_mov_b32_e32 v60, v240
	v_mov_b32_e32 v61, v241
	v_mov_b32_e32 v62, v234
	v_mov_b32_e32 v63, v235
	v_mov_b32_e32 v64, v236
	v_mov_b32_e32 v65, v237

.LBB0_1226:
	s_or_saveexec_b64 s[18:19], s[18:19]
	v_or_b32_e32 v34, 1, v70
	v_ashrrev_i32_e32 v35, 31, v34
	v_lshlrev_b64 v[34:35], 11, v[34:35]
	v_lshl_add_u64 v[74:75], v[68:69], 0, v[34:35]
	s_xor_b64 exec, exec, s[18:19]
	s_cbranch_execz .LBB0_1228
	s_cmp_lg_u32 s20, 0
	s_cbranch_scc1 .Lbn_mv1
	global_load_dwordx4 v[50:53], v[74:75], off offset:16
	global_load_dwordx4 v[54:57], v[74:75], off
	s_branch .LBB0_1228
.Lbn_mv1:
	v_mov_b32_e32 v50, v246
	v_mov_b32_e32 v51, v247
	v_mov_b32_e32 v52, v248
	v_mov_b32_e32 v53, v249
	v_mov_b32_e32 v54, v242
	v_mov_b32_e32 v55, v243
	v_mov_b32_e32 v56, v244
	v_mov_b32_e32 v57, v245

.LBB0_1230:
	s_or_saveexec_b64 s[18:19], s[18:19]
	v_or_b32_e32 v34, 2, v70
	v_ashrrev_i32_e32 v35, 31, v34
	v_lshlrev_b64 v[34:35], 11, v[34:35]
	v_lshl_add_u64 v[72:73], v[68:69], 0, v[34:35]
	s_xor_b64 exec, exec, s[18:19]
	s_cbranch_execz .LBB0_1232
	s_cmp_lg_u32 s20, 0
	s_cbranch_scc1 .Lbn_mv2
	global_load_dwordx4 v[42:45], v[72:73], off offset:16
	global_load_dwordx4 v[46:49], v[72:73], off
	s_branch .LBB0_1232
.Lbn_mv2:
	v_mov_b32_e32 v42, v226
	v_mov_b32_e32 v43, v227
	v_mov_b32_e32 v44, v228
	v_mov_b32_e32 v45, v229
	v_mov_b32_e32 v46, v222
	v_mov_b32_e32 v47, v223
	v_mov_b32_e32 v48, v224
	v_mov_b32_e32 v49, v225

.LBB0_1234:
	s_or_saveexec_b64 s[18:19], s[18:19]
	v_or_b32_e32 v70, 3, v70
	v_ashrrev_i32_e32 v71, 31, v70
	v_lshlrev_b64 v[70:71], 11, v[70:71]
	v_lshl_add_u64 v[70:71], v[68:69], 0, v[70:71]
	s_xor_b64 exec, exec, s[18:19]
	s_cbranch_execz .LBB0_1236
	s_cmp_lg_u32 s20, 0
	s_cbranch_scc1 .Lbn_mv3
	global_load_dwordx4 v[34:37], v[70:71], off offset:16
	global_load_dwordx4 v[38:41], v[70:71], off
	s_branch .LBB0_1236
.Lbn_mv3:
	v_mov_b32_e32 v34, v122
	v_mov_b32_e32 v35, v123
	v_mov_b32_e32 v36, v124
	v_mov_b32_e32 v37, v125
	v_mov_b32_e32 v38, v250
	v_mov_b32_e32 v39, v251
	v_mov_b32_e32 v40, v252
	v_mov_b32_e32 v41, v253
.LBB0_1236:
	s_or_b64 exec, exec, s[18:19]
	s_cmp_lg_u32 s20, 0
	s_cbranch_scc1 .Lbn_nopf
	s_mov_b64 s[18:19], exec
	s_andn2_b64 exec, exec, s[6:7]
	s_cbranch_execz .Lbn_pfx
	v_lshl_add_u64 v[234:235], v[76:77], 0, s[100:101]
	global_load_dwordx4 v[238:241], v[234:235], off offset:16
	s_nop 0
	global_load_dwordx4 v[234:237], v[234:235], off
	v_lshl_add_u64 v[242:243], v[74:75], 0, s[100:101]
	global_load_dwordx4 v[246:249], v[242:243], off offset:16
	s_nop 0
	global_load_dwordx4 v[242:245], v[242:243], off
	v_lshl_add_u64 v[222:223], v[72:73], 0, s[100:101]
	global_load_dwordx4 v[226:229], v[222:223], off offset:16
	s_nop 0
	global_load_dwordx4 v[222:225], v[222:223], off
	v_lshl_add_u64 v[250:251], v[70:71], 0, s[100:101]
	global_load_dwordx4 v[122:125], v[250:251], off offset:16
	s_nop 0
	global_load_dwordx4 v[250:253], v[250:251], off
.Lbn_pfx:
	s_mov_b64 exec, s[18:19]
.Lbn_nopf:
	s_waitcnt vmcnt(8)
	v_lshlrev_b32_e32 v78, 16, v62
	v_and_b32_e32 v79, 0xffff0000, v62
	v_lshlrev_b32_e32 v62, 16, v63
	v_and_b32_e32 v63, 0xffff0000, v63
	v_pk_mul_f32 v[106:107], v[78:79], v[78:79]
	v_pk_mul_f32 v[108:109], v[62:63], v[62:63]
	v_add_f32_e32 v105, v106, v107
	v_lshlrev_b32_e32 v80, 16, v64
	v_and_b32_e32 v81, 0xffff0000, v64
	v_add_f32_e32 v105, v108, v105
	v_pk_mul_f32 v[110:111], v[80:81], v[80:81]
	v_add_f32_e32 v105, v109, v105
	v_lshlrev_b32_e32 v64, 16, v65
	v_and_b32_e32 v65, 0xffff0000, v65
	v_add_f32_e32 v105, v110, v105
	v_pk_mul_f32 v[112:113], v[64:65], v[64:65]
	v_add_f32_e32 v105, v111, v105
	v_lshlrev_b32_e32 v82, 16, v58
	v_and_b32_e32 v83, 0xffff0000, v58
	v_add_f32_e32 v105, v112, v105
	v_pk_mul_f32 v[114:115], v[82:83], v[82:83]
	v_add_f32_e32 v105, v113, v105
	v_lshlrev_b32_e32 v58, 16, v59
	v_and_b32_e32 v59, 0xffff0000, v59
	v_add_f32_e32 v105, v114, v105
	v_pk_mul_f32 v[116:117], v[58:59], v[58:59]
	v_add_f32_e32 v105, v115, v105
	v_lshlrev_b32_e32 v84, 16, v60
	v_and_b32_e32 v85, 0xffff0000, v60
	v_add_f32_e32 v105, v116, v105
	v_pk_mul_f32 v[118:119], v[84:85], v[84:85]
	v_add_f32_e32 v105, v117, v105
	v_lshlrev_b32_e32 v60, 16, v61
	v_and_b32_e32 v61, 0xffff0000, v61
	v_add_f32_e32 v105, v118, v105
	v_pk_mul_f32 v[120:121], v[60:61], v[60:61]
	v_add_f32_e32 v105, v119, v105
	v_add_f32_e32 v105, v120, v105
	v_add_f32_e32 v105, v121, v105
	s_nop 1
	v_add_f32_dpp v105, v105, v105 quad_perm:[1,0,3,2] row_mask:0xf bank_mask:0xf bound_ctrl:1
	s_nop 1
	v_add_f32_dpp v105, v105, v105 quad_perm:[2,3,0,1] row_mask:0xf bank_mask:0xf bound_ctrl:1
	s_nop 1
	v_add_f32_dpp v105, v105, v105 row_half_mirror row_mask:0xf bank_mask:0xf bound_ctrl:1
	s_nop 0
	v_readlane_b32 s25, v105, 0
	v_readlane_b32 s26, v105, 8
	v_readlane_b32 s27, v105, 16
	v_readlane_b32 s29, v105, 24
	v_readlane_b32 s28, v105, 32
	v_readlane_b32 s30, v105, 40
	v_readlane_b32 s34, v105, 48
	v_readlane_b32 s31, v105, 56
	s_and_saveexec_b64 s[18:19], s[8:9]
	s_xor_b64 s[18:19], exec, s[18:19]
	s_cbranch_execz .LBB0_1242
	s_and_saveexec_b64 s[20:21], s[10:11]
	s_xor_b64 s[20:21], exec, s[20:21]
	v_mov_b32_e32 v105, s34
	v_add_f32_e32 v105, s30, v105
	v_add_f32_e32 v105, s31, v105
	v_mul_f32_e32 v105, 0x3b2aaaab, v105
	s_andn2_saveexec_b64 s[20:21], s[20:21]
	v_mov_b32_e32 v105, s29
	v_add_f32_e32 v105, s27, v105
	v_add_f32_e32 v105, s28, v105
	v_mul_f32_e32 v105, 0x3b2aaaab, v105
	s_or_b64 exec, exec, s[20:21]
